# grid barrier: non-leader workgroups poll the global generation word (TOPGEN) directly instead of waiting for their XCD leader to republish it in the per-XCD generation word; one memory round trip less
# baseline (speedup 1.0000x reference)
.LBB0_125:
	s_or_b64 exec, exec, s[6:7]
	v_cvt_f32_u32_e32 v5, v3
	s_waitcnt vmcnt(0)
	v_readfirstlane_b32 s4, v4
	v_sub_u32_e32 v4, 0, v3
	v_rcp_iflag_f32_e32 v5, v5
	v_add_u32_e32 v6, s4, v2
	v_mul_f32_e32 v5, 0x4f7ffffe, v5
	v_cvt_u32_f32_e32 v5, v5
	v_mul_lo_u32 v2, v4, v5
	v_mul_hi_u32 v2, v5, v2
	v_add_u32_e32 v2, v5, v2
	v_mul_hi_u32 v2, v6, v2
	v_mul_lo_u32 v4, v2, v3
	v_sub_u32_e32 v4, v6, v4
	v_add_u32_e32 v5, 1, v2
	v_cmp_ge_u32_e32 vcc, v4, v3
	s_nop 1
	v_cndmask_b32_e32 v2, v2, v5, vcc
	v_sub_u32_e32 v5, v4, v3
	v_cndmask_b32_e32 v4, v4, v5, vcc
	v_add_u32_e32 v5, 1, v2
	v_cmp_ge_u32_e32 vcc, v4, v3
	v_add_u32_e32 v4, 1, v6
	s_nop 0
	v_cndmask_b32_e32 v2, v2, v5, vcc
	v_mul_lo_u32 v5, v3, v2
	v_add_u32_e32 v3, v5, v3
	v_cmp_ne_u32_e32 vcc, v4, v3
	s_and_saveexec_b64 s[4:5], vcc
	s_xor_b64 s[4:5], exec, s[4:5]
	s_cbranch_execz .LBB0_139
	s_movk_i32 s6, 0xd40
	s_mov_b32 s7, 0
	s_lshl_b64 s[6:7], s[6:7], 2
	s_add_u32 s8, s54, s6
	s_addc_u32 s9, s55, s7
	s_waitcnt lgkmcnt(0)
	v_mov_b32_e32 v1, 0
	global_load_dword v3, v1, s[8:9] sc1
	s_waitcnt vmcnt(0)
	v_cmp_eq_u32_e32 vcc, v3, v2
	s_and_saveexec_b64 s[6:7], vcc
	s_cbranch_execz .LBB0_138
	s_mov_b32 s20, 1
	s_mov_b64 s[10:11], 0
	s_branch .LBB0_129

.LBB0_224:
	s_or_b64 exec, exec, s[6:7]
	v_cvt_f32_u32_e32 v6, v4
	s_waitcnt vmcnt(0)
	v_readfirstlane_b32 s4, v5
	v_sub_u32_e32 v5, 0, v4
	v_rcp_iflag_f32_e32 v6, v6
	v_add_u32_e32 v7, s4, v3
	v_mul_f32_e32 v6, 0x4f7ffffe, v6
	v_cvt_u32_f32_e32 v6, v6
	v_mul_lo_u32 v3, v5, v6
	v_mul_hi_u32 v3, v6, v3
	v_add_u32_e32 v3, v6, v3
	v_mul_hi_u32 v3, v7, v3
	v_mul_lo_u32 v5, v3, v4
	v_sub_u32_e32 v5, v7, v5
	v_add_u32_e32 v6, 1, v3
	v_cmp_ge_u32_e32 vcc, v5, v4
	s_nop 1
	v_cndmask_b32_e32 v3, v3, v6, vcc
	v_sub_u32_e32 v6, v5, v4
	v_cndmask_b32_e32 v5, v5, v6, vcc
	v_add_u32_e32 v6, 1, v3
	v_cmp_ge_u32_e32 vcc, v5, v4
	v_add_u32_e32 v5, 1, v7
	s_nop 0
	v_cndmask_b32_e32 v3, v3, v6, vcc
	v_mul_lo_u32 v6, v4, v3
	v_add_u32_e32 v4, v6, v4
	v_cmp_ne_u32_e32 vcc, v5, v4
	s_and_saveexec_b64 s[4:5], vcc
	s_xor_b64 s[4:5], exec, s[4:5]
	s_cbranch_execz .LBB0_238
	s_movk_i32 s6, 0xd40
	s_mov_b32 s7, s56
	s_lshl_b64 s[6:7], s[6:7], 2
	s_add_u32 s8, s54, s6
	s_addc_u32 s9, s55, s7
	s_waitcnt lgkmcnt(0)
	global_load_dword v2, v227, s[8:9] sc1
	s_waitcnt vmcnt(0)
	v_cmp_eq_u32_e32 vcc, v2, v3
	s_and_saveexec_b64 s[6:7], vcc
	s_cbranch_execz .LBB0_237
	s_mov_b32 s21, 1
	s_mov_b64 s[10:11], 0
	s_branch .LBB0_228
